# grid barrier: XCD leader bumps the per-XCD generation before its own L1 invalidate (non-leaders released ~1 invalidate latency earlier at each of 20 seams)
# baseline (speedup 1.0000x reference)
.LBB0_222:
	s_or_b64 exec, exec, s[2:3]
	s_waitcnt vmcnt(0)
	global_atomic_add v[170:171], v187, off
	buffer_inv sc1
	s_waitcnt vmcnt(0)
